# P6 epilogue: placeholder loads removed, every counted vmcnt wait re-derived from the real outstanding-op history
# speedup vs baseline: 1.0096x; 1.0002x over previous
.LBB0_975:
	s_add_i32 s0, s96, s35
	s_ashr_i32 s1, s0, 31
	s_lshr_b32 s1, s1, 19
	s_add_i32 s0, s0, s1
	s_ashr_i32 s2, s0, 13
	s_xor_b64 s[14:15], s[6:7], -1
	s_ashr_i32 s0, s2, 31
	s_add_u32 s1, s2, s87
	s_addc_u32 s0, s0, 0
	s_waitcnt vmcnt(0)
	v_lshlrev_b32_e32 v186, 6, v179
	v_lshl_add_u32 v185, v179, 4, s85
	v_mov_b32_e32 v187, 0
	global_load_dwordx4 v[8:11], v186, s[16:17] offset:0
	global_load_dwordx4 v[12:15], v186, s[16:17] offset:16
	global_load_dwordx4 v[16:19], v186, s[16:17] offset:32
	global_load_dwordx4 v[20:23], v186, s[16:17] offset:48
	global_load_dwordx4 v[24:27], v186, s[28:29] offset:0
	global_load_dwordx4 v[28:31], v186, s[28:29] offset:16
	global_load_dwordx4 v[32:35], v186, s[28:29] offset:32
	global_load_dwordx4 v[36:39], v186, s[28:29] offset:48
	global_load_dwordx4 v[40:43], v186, s[12:13] offset:0
	global_load_dwordx4 v[44:47], v186, s[12:13] offset:16
	global_load_dwordx4 v[48:51], v186, s[12:13] offset:32
	global_load_dwordx4 v[52:55], v186, s[12:13] offset:48
	global_load_dwordx4 v[56:59], v186, s[90:91] offset:0
	global_load_dwordx4 v[60:63], v186, s[90:91] offset:16
	global_load_dwordx4 v[64:67], v186, s[90:91] offset:32
	global_load_dwordx4 v[68:71], v186, s[90:91] offset:48
	s_waitcnt vmcnt(0)
	ds_write_b128 v185, v[8:11] offset:0
	ds_write_b128 v185, v[12:15] offset:1024
	ds_write_b128 v185, v[16:19] offset:2048
	ds_write_b128 v185, v[20:23] offset:3072
	ds_write_b128 v185, v[24:27] offset:4096
	ds_write_b128 v185, v[28:31] offset:5120
	ds_write_b128 v185, v[32:35] offset:6144
	ds_write_b128 v185, v[36:39] offset:7168
	ds_write_b128 v185, v[40:43] offset:8192
	ds_write_b128 v185, v[44:47] offset:9216
	ds_write_b128 v185, v[48:51] offset:10240
	ds_write_b128 v185, v[52:55] offset:11264
	ds_write_b128 v185, v[56:59] offset:12288
	ds_write_b128 v185, v[60:63] offset:13312
	ds_write_b128 v185, v[64:67] offset:14336
	ds_write_b128 v185, v[68:71] offset:15360
	s_waitcnt lgkmcnt(0)
	s_mul_i32 s40, s1, 0x6000
	s_add_u32 s40, s70, s40
	s_addc_u32 s41, s71, 0
	s_add_u32 s42, s40, 0x5000
	s_addc_u32 s43, s41, 0
	s_add_u32 s40, s40, 0x18000
	s_addc_u32 s41, s41, 0
	v_mov_b32_e32 v188, 0x10000
	v_lshl_add_u32 v188, v179, 4, v188
	global_load_dwordx4 v[8:11], v186, s[42:43] offset:0
	global_load_dwordx4 v[12:15], v186, s[42:43] offset:16
	global_load_dwordx4 v[16:19], v186, s[42:43] offset:32
	global_load_dwordx4 v[20:23], v186, s[42:43] offset:48
	global_load_dwordx4 v[24:27], v186, s[40:41] offset:0
	global_load_dwordx4 v[28:31], v186, s[40:41] offset:16
	global_load_dwordx4 v[32:35], v186, s[40:41] offset:32
	global_load_dwordx4 v[36:39], v186, s[40:41] offset:48
	s_waitcnt vmcnt(0)
	ds_write_b128 v188, v[8:11] offset:0
	ds_write_b128 v188, v[12:15] offset:1024
	ds_write_b128 v188, v[16:19] offset:2048
	ds_write_b128 v188, v[20:23] offset:3072
	ds_write_b128 v188, v[24:27] offset:4096
	ds_write_b128 v188, v[28:31] offset:5120
	ds_write_b128 v188, v[32:35] offset:6144
	ds_write_b128 v188, v[36:39] offset:7168
	s_waitcnt lgkmcnt(0)
	v_readlane_b32 s40, v253, 62
	v_readlane_b32 s41, v253, 63
	s_lshl_b64 s[44:45], s[96:97], 12
	v_lshlrev_b32_e32 v2, 6, v179
	s_add_u32 s40, s40, s44
	s_addc_u32 s41, s41, s45
	s_add_u32 s40, s40, 0x1000
	s_addc_u32 s41, s41, 0
	global_load_dword v184, v2, s[40:41]
	s_add_u32 s40, s40, 0x1000
	s_addc_u32 s41, s41, 0
	global_load_dword v184, v2, s[40:41]
	s_add_u32 s40, s40, 0x1000
	s_addc_u32 s41, s41, 0
	global_load_dword v184, v2, s[40:41]
	v_mov_b32_e32 v1, v179
	s_mulk_i32 s0, 0x6000
	s_mul_hi_u32 s3, s1, 0x6000
	s_add_i32 s3, s3, s0
	s_mulk_i32 s1, 0x6000
	v_lshlrev_b32_e32 v20, 4, v1
	s_add_u32 s6, s70, s1
	v_readlane_b32 s36, v253, 60
	v_ashrrev_i32_e32 v21, 31, v20
	s_addc_u32 s7, s71, s3
	s_lshl_b64 s[0:1], s[96:97], 12
	v_readlane_b32 s38, v253, 62
	v_lshlrev_b64 v[22:23], 2, v[20:21]
	v_readlane_b32 s39, v253, 63
	s_add_u32 s20, s38, s0
	v_lshl_add_u64 v[68:69], s[6:7], 0, v[22:23]
	s_mov_b64 s[6:7], 0x5000
	s_addc_u32 s21, s39, s1
	v_lshl_add_u64 v[12:13], v[68:69], 0, s[6:7]
	s_lshl_b64 s[6:7], s[96:97], 3
	v_lshl_add_u64 v[32:33], s[20:21], 0, v[22:23]
	s_add_u32 s6, s64, s6
	ds_read_b128 v[4:7], v188 offset:3072
	ds_read_b128 v[8:11], v188 offset:2048
	s_addc_u32 s7, s65, s7
	ds_read_b128 v[12:15], v188 offset:1024
	s_nop 0
	global_load_dwordx2 v[72:73], v3, s[6:7]
	global_load_dwordx4 v[16:19], v[32:33], off
	global_load_dwordx4 v[24:27], v[32:33], off offset:16
	global_load_dwordx4 v[28:31], v[32:33], off offset:32
	s_nop 0
	global_load_dwordx4 v[32:35], v[32:33], off offset:48
	v_lshl_add_u64 v[60:61], s[16:17], 0, v[22:23]
	v_lshl_add_u64 v[64:65], s[28:29], 0, v[22:23]
	v_add_co_u32_e32 v68, vcc, s18, v68
	ds_read_b128 v[36:39], v185 offset:7168
	ds_read_b128 v[40:43], v185 offset:3072
	ds_read_b128 v[44:47], v185 offset:2048
	ds_read_b128 v[48:51], v185 offset:6144
	ds_read_b128 v[52:55], v185 offset:5120
	ds_read_b128 v[56:59], v185 offset:1024
	s_nop 0
	ds_read_b128 v[60:63], v185 offset:0
	s_nop 0
	ds_read_b128 v[64:67], v185 offset:4096
	v_addc_co_u32_e32 v69, vcc, 0, v69, vcc
	ds_read_b128 v[68:71], v188 offset:0
	v_add_u32_e32 v142, 64, v183
	v_xor_b32_e32 v1, 1, v178
	v_xor_b32_e32 v2, 2, v178
	v_cmp_lt_i32_e32 vcc, v1, v142
	v_xor_b32_e32 v74, 4, v178
	v_readlane_b32 s20, v255, 42
	v_cndmask_b32_e32 v1, v178, v1, vcc
	v_cmp_lt_i32_e32 vcc, v2, v142
	v_readlane_b32 s22, v255, 44
	s_add_u32 s0, s30, s0
	v_cndmask_b32_e32 v75, v178, v2, vcc
	v_lshlrev_b32_e32 v2, 2, v1
	v_lshlrev_b32_e32 v1, 2, v75
	v_cmp_lt_i32_e32 vcc, v74, v142
	s_addc_u32 s1, s31, s1
	v_readlane_b32 s37, v253, 61
	v_readlane_b32 s40, v254, 0
	v_readlane_b32 s41, v254, 1
	v_readlane_b32 s42, v254, 2
	v_readlane_b32 s43, v254, 3
	v_readlane_b32 s44, v254, 4
	v_readlane_b32 s45, v254, 5
	v_readlane_b32 s46, v254, 6
	v_readlane_b32 s47, v254, 7
	v_readlane_b32 s48, v254, 8
	v_readlane_b32 s49, v254, 9
	v_readlane_b32 s50, v254, 10
	v_readlane_b32 s51, v254, 11
	v_readlane_b32 s21, v255, 43
	v_readlane_b32 s23, v255, 45
	s_waitcnt lgkmcnt(0)
	s_waitcnt vmcnt(5)
	v_pk_add_f32 v[12:13], v[12:13], 1.0 op_sel_hi:[1,0]
	v_pk_add_f32 v[14:15], v[14:15], 1.0 op_sel_hi:[1,0]
	s_waitcnt lgkmcnt(0)
	s_waitcnt vmcnt(3)
	v_pk_add_f32 v[18:19], v[18:19], v[72:73] op_sel_hi:[1,0] neg_lo:[0,1] neg_hi:[0,1]
	v_pk_add_f32 v[4:5], v[4:5], 1.0 op_sel_hi:[1,0]
	v_pk_mul_f32 v[18:19], v[72:73], v[18:19] op_sel:[1,0]
	s_waitcnt lgkmcnt(0)
	s_waitcnt vmcnt(0)
	v_pk_add_f32 v[32:33], v[32:33], v[72:73] op_sel_hi:[1,0] neg_lo:[0,1] neg_hi:[0,1]
	v_pk_add_f32 v[34:35], v[34:35], v[72:73] op_sel_hi:[1,0] neg_lo:[0,1] neg_hi:[0,1]
	v_pk_mul_f32 v[32:33], v[72:73], v[32:33] op_sel:[1,0]
	v_pk_mul_f32 v[34:35], v[72:73], v[34:35] op_sel:[1,0]
	s_waitcnt lgkmcnt(0)
	s_waitcnt vmcnt(0)
	v_pk_fma_f32 v[32:33], v[32:33], v[40:41], v[36:37]
	v_pk_fma_f32 v[34:35], v[34:35], v[42:43], v[38:39]
	v_pk_mul_f32 v[32:33], v[32:33], s[34:35] op_sel_hi:[1,0]
	v_pk_add_f32 v[6:7], v[6:7], 1.0 op_sel_hi:[1,0]
	v_pk_add_f32 v[24:25], v[24:25], v[72:73] op_sel_hi:[1,0] neg_lo:[0,1] neg_hi:[0,1]
	v_pk_mul_f32 v[34:35], v[34:35], s[34:35] op_sel_hi:[1,0]
	v_pk_fma_f32 v[42:43], v[138:139], v[4:5], v[32:33]
	s_waitcnt lgkmcnt(0)
	s_waitcnt vmcnt(0)
	v_pk_fma_f32 v[4:5], v[18:19], v[62:63], v[66:67]
	v_pk_add_f32 v[16:17], v[16:17], v[72:73] op_sel_hi:[1,0] neg_lo:[0,1] neg_hi:[0,1]
	v_pk_mul_f32 v[24:25], v[72:73], v[24:25] op_sel:[1,0]
	v_pk_fma_f32 v[40:41], v[140:141], v[6:7], v[34:35]
	v_pk_mul_f32 v[4:5], v[4:5], s[34:35] op_sel_hi:[1,0]
	s_waitcnt lgkmcnt(0)
	s_waitcnt vmcnt(0)
	v_pk_add_f32 v[6:7], v[70:71], 1.0 op_sel_hi:[1,0]
	v_pk_fma_f32 v[24:25], v[24:25], v[56:57], v[52:53]
	v_pk_fma_f32 v[52:53], v[128:129], v[6:7], v[4:5]
	v_pk_mul_f32 v[4:5], v[72:73], v[16:17] op_sel:[1,0]
	v_pk_add_f32 v[26:27], v[26:27], v[72:73] op_sel_hi:[1,0] neg_lo:[0,1] neg_hi:[0,1]
	v_pk_fma_f32 v[4:5], v[60:61], v[4:5], v[64:65]
	v_pk_mul_f32 v[26:27], v[72:73], v[26:27] op_sel:[1,0]
	v_pk_mul_f32 v[4:5], v[4:5], s[34:35] op_sel_hi:[1,0]
	v_pk_add_f32 v[6:7], v[68:69], 1.0 op_sel_hi:[1,0]
	v_pk_fma_f32 v[26:27], v[26:27], v[58:59], v[54:55]
	v_pk_fma_f32 v[54:55], v[126:127], v[6:7], v[4:5]
	v_pk_add_f32 v[30:31], v[30:31], v[72:73] op_sel_hi:[1,0] neg_lo:[0,1] neg_hi:[0,1]
	v_add_f32_e32 v4, 0, v54
	v_add_f32_e32 v4, v4, v55
	v_pk_mul_f32 v[30:31], v[72:73], v[30:31] op_sel:[1,0]
	v_pk_mul_f32 v[24:25], v[24:25], s[34:35] op_sel_hi:[1,0]
	v_add_f32_e32 v4, v4, v52
	v_pk_add_f32 v[28:29], v[28:29], v[72:73] op_sel_hi:[1,0] neg_lo:[0,1] neg_hi:[0,1]
	v_pk_fma_f32 v[30:31], v[30:31], v[46:47], v[50:51]
	v_pk_fma_f32 v[50:51], v[130:131], v[12:13], v[24:25]
	v_add_f32_e32 v4, v4, v53
	v_pk_mul_f32 v[28:29], v[72:73], v[28:29] op_sel:[1,0]
	v_pk_mul_f32 v[26:27], v[26:27], s[34:35] op_sel_hi:[1,0]
	v_add_f32_e32 v4, v4, v50
	v_pk_fma_f32 v[28:29], v[28:29], v[44:45], v[48:49]
	v_pk_fma_f32 v[48:49], v[132:133], v[14:15], v[26:27]
	v_add_f32_e32 v4, v4, v51
	v_pk_add_f32 v[8:9], v[8:9], 1.0 op_sel_hi:[1,0]
	v_pk_mul_f32 v[28:29], v[28:29], s[34:35] op_sel_hi:[1,0]
	v_add_f32_e32 v4, v4, v48
	v_pk_fma_f32 v[46:47], v[134:135], v[8:9], v[28:29]
	v_add_f32_e32 v4, v4, v49
	v_pk_add_f32 v[10:11], v[10:11], 1.0 op_sel_hi:[1,0]
	v_pk_mul_f32 v[30:31], v[30:31], s[34:35] op_sel_hi:[1,0]
	v_add_f32_e32 v4, v4, v46
	v_pk_fma_f32 v[44:45], v[136:137], v[10:11], v[30:31]
	v_add_f32_e32 v4, v4, v47
	v_add_f32_e32 v4, v4, v44
	v_add_f32_e32 v4, v4, v45
	v_add_f32_e32 v4, v4, v42
	v_add_f32_e32 v4, v4, v43
	v_add_f32_e32 v4, v4, v40
	v_add_f32_e32 v4, v4, v41
	ds_bpermute_b32 v5, v2, v4
	v_cndmask_b32_e32 v6, v178, v74, vcc
	v_lshlrev_b32_e32 v74, 2, v6
	v_xor_b32_e32 v6, 8, v178
	v_cmp_lt_i32_e32 vcc, v6, v142
	s_waitcnt lgkmcnt(0)
	v_add_f32_e32 v4, v4, v5
	ds_bpermute_b32 v5, v1, v4
	v_cndmask_b32_e32 v6, v178, v6, vcc
	v_lshlrev_b32_e32 v75, 2, v6
	v_xor_b32_e32 v6, 16, v178
	v_cmp_lt_i32_e32 vcc, v6, v142
	s_waitcnt lgkmcnt(0)
	v_add_f32_e32 v4, v4, v5
	ds_bpermute_b32 v5, v74, v4
	v_cndmask_b32_e32 v6, v178, v6, vcc
	v_lshlrev_b32_e32 v126, 2, v6
	v_xor_b32_e32 v6, 32, v178
	v_cmp_lt_i32_e32 vcc, v6, v142
	s_waitcnt lgkmcnt(0)
	v_add_f32_e32 v7, v4, v5
	ds_bpermute_b32 v8, v75, v7
	v_cndmask_b32_e32 v4, v178, v6, vcc
	v_lshlrev_b32_e32 v127, 2, v4
	v_lshl_add_u64 v[4:5], s[12:13], 0, v[22:23]
	v_lshl_add_u64 v[36:37], s[90:91], 0, v[22:23]
	s_waitcnt lgkmcnt(0)
	v_add_f32_e32 v24, v7, v8
	ds_bpermute_b32 v25, v126, v24
	ds_read_b128 v[16:19], v185 offset:11264
	ds_read_b128 v[12:15], v185 offset:10240
	ds_read_b128 v[8:11], v185 offset:9216
	s_nop 0
	ds_read_b128 v[4:7], v185 offset:8192
	v_lshl_add_u64 v[22:23], s[0:1], 0, v[22:23]
	v_readlane_b32 s0, v255, 23
	v_readlane_b32 s1, v255, 24
	s_waitcnt lgkmcnt(0)
	v_add_f32_e32 v56, v24, v25
	ds_read_b128 v[24:27], v185 offset:15360
	ds_read_b128 v[28:31], v185 offset:14336
	ds_read_b128 v[32:35], v185 offset:13312
	s_nop 0
	ds_read_b128 v[36:39], v185 offset:12288
	ds_bpermute_b32 v57, v127, v56
	s_waitcnt lgkmcnt(0)
	v_add_f32_e32 v56, v56, v57
	v_mul_f32_e32 v56, 0x3a800000, v56
	v_pk_add_f32 v[54:55], v[54:55], v[56:57] op_sel_hi:[1,0] neg_lo:[0,1] neg_hi:[0,1]
	v_pk_add_f32 v[52:53], v[52:53], v[56:57] op_sel_hi:[1,0] neg_lo:[0,1] neg_hi:[0,1]
	v_pk_mul_f32 v[58:59], v[54:55], v[54:55]
	v_pk_mul_f32 v[60:61], v[52:53], v[52:53]
	v_add_f32_e32 v58, v58, v59
	v_pk_add_f32 v[50:51], v[50:51], v[56:57] op_sel_hi:[1,0] neg_lo:[0,1] neg_hi:[0,1]
	v_add_f32_e32 v58, v60, v58
	v_pk_mul_f32 v[62:63], v[50:51], v[50:51]
	v_add_f32_e32 v58, v61, v58
	v_pk_add_f32 v[48:49], v[48:49], v[56:57] op_sel_hi:[1,0] neg_lo:[0,1] neg_hi:[0,1]
	v_add_f32_e32 v58, v62, v58
	v_pk_mul_f32 v[64:65], v[48:49], v[48:49]
	v_add_f32_e32 v58, v63, v58
	v_pk_add_f32 v[46:47], v[46:47], v[56:57] op_sel_hi:[1,0] neg_lo:[0,1] neg_hi:[0,1]
	v_add_f32_e32 v58, v64, v58
	v_pk_mul_f32 v[66:67], v[46:47], v[46:47]
	v_add_f32_e32 v58, v65, v58
	v_pk_add_f32 v[44:45], v[44:45], v[56:57] op_sel_hi:[1,0] neg_lo:[0,1] neg_hi:[0,1]
	v_add_f32_e32 v58, v66, v58
	v_pk_mul_f32 v[68:69], v[44:45], v[44:45]
	v_add_f32_e32 v58, v67, v58
	v_pk_add_f32 v[42:43], v[42:43], v[56:57] op_sel_hi:[1,0] neg_lo:[0,1] neg_hi:[0,1]
	v_add_f32_e32 v58, v68, v58
	v_pk_mul_f32 v[70:71], v[42:43], v[42:43]
	v_add_f32_e32 v58, v69, v58
	v_pk_add_f32 v[40:41], v[40:41], v[56:57] op_sel_hi:[1,0] neg_lo:[0,1] neg_hi:[0,1]
	v_add_f32_e32 v58, v70, v58
	v_pk_mul_f32 v[56:57], v[40:41], v[40:41]
	v_add_f32_e32 v58, v71, v58
	v_add_f32_e32 v56, v56, v58
	v_add_f32_e32 v56, v57, v56
	ds_bpermute_b32 v57, v2, v56
	s_waitcnt lgkmcnt(0)
	v_add_f32_e32 v56, v56, v57
	ds_bpermute_b32 v57, v1, v56
	s_waitcnt lgkmcnt(0)
	v_add_f32_e32 v56, v56, v57
	ds_bpermute_b32 v57, v74, v56
	s_waitcnt lgkmcnt(0)
	v_add_f32_e32 v56, v56, v57
	ds_bpermute_b32 v57, v75, v56
	s_waitcnt lgkmcnt(0)
	v_add_f32_e32 v56, v56, v57
	ds_bpermute_b32 v57, v126, v56
	s_waitcnt lgkmcnt(0)
	v_add_f32_e32 v56, v56, v57
	ds_bpermute_b32 v57, v127, v56
	s_waitcnt lgkmcnt(0)
	v_add_f32_e32 v56, v56, v57
	v_fmamk_f32 v56, v56, 0x3a800000, v204
	v_mul_f32_e32 v57, 0x4b800000, v56
	v_cmp_gt_f32_e32 vcc, s22, v56
	s_nop 1
	v_cndmask_b32_e32 v56, v56, v57, vcc
	v_rsq_f32_e32 v56, v56
	s_nop 0
	v_mul_f32_e32 v57, 0x45800000, v56
	v_cndmask_b32_e32 v56, v56, v57, vcc
	v_pk_mul_f32 v[54:55], v[54:55], v[56:57] op_sel_hi:[1,0]
	v_pk_mul_f32 v[52:53], v[52:53], v[56:57] op_sel_hi:[1,0]
	s_waitcnt lgkmcnt(0)
	s_waitcnt vmcnt(0)
	v_pk_fma_f32 v[4:5], v[4:5], v[54:55], v[36:37]
	v_pk_mul_f32 v[36:37], v[50:51], v[56:57] op_sel_hi:[1,0]
	v_pk_fma_f32 v[6:7], v[6:7], v[52:53], v[38:39]
	v_pk_fma_f32 v[8:9], v[8:9], v[36:37], v[32:33]
	v_pk_mul_f32 v[32:33], v[48:49], v[56:57] op_sel_hi:[1,0]
	s_and_b64 vcc, exec, s[0:1]
	v_pk_fma_f32 v[10:11], v[10:11], v[32:33], v[34:35]
	v_pk_mul_f32 v[32:33], v[46:47], v[56:57] op_sel_hi:[1,0]
	s_nop 0
	v_pk_fma_f32 v[12:13], v[12:13], v[32:33], v[28:29]
	v_pk_mul_f32 v[28:29], v[44:45], v[56:57] op_sel_hi:[1,0]
	s_nop 0
	v_pk_fma_f32 v[14:15], v[14:15], v[28:29], v[30:31]
	v_pk_mul_f32 v[28:29], v[42:43], v[56:57] op_sel_hi:[1,0]
	s_nop 0
	v_pk_fma_f32 v[16:17], v[16:17], v[28:29], v[24:25]
	v_pk_mul_f32 v[24:25], v[40:41], v[56:57] op_sel_hi:[1,0]
	s_nop 0
	v_pk_fma_f32 v[18:19], v[18:19], v[24:25], v[26:27]
	global_store_dwordx4 v[22:23], v[4:7], off
	global_store_dwordx4 v[22:23], v[8:11], off offset:16
	global_store_dwordx4 v[22:23], v[12:15], off offset:32
	global_store_dwordx4 v[22:23], v[16:19], off offset:48
	s_cbranch_vccz .LBB0_977
	s_lshl_b64 s[0:1], s[96:97], 10
	s_mul_hi_i32 s3, s2, 0x6000
	s_mulk_i32 s2, 0x6000
	s_add_u32 s2, s70, s2
	s_addc_u32 s3, s71, s3
	v_lshl_add_u64 v[50:51], v[20:21], 2, s[2:3]
	s_mov_b64 s[2:3], 0x19000
	v_add_co_u32_e32 v34, vcc, s86, v50
	v_lshl_add_u64 v[30:31], v[50:51], 0, s[2:3]
	s_mov_b64 s[2:3], 0x18000
	v_addc_co_u32_e32 v35, vcc, 0, v51, vcc
	v_lshl_add_u64 v[46:47], v[50:51], 0, s[2:3]
	v_add_co_u32_e32 v50, vcc, s67, v50
	global_load_dwordx4 v[22:25], v[30:31], off offset:32
	global_load_dwordx4 v[26:29], v[30:31], off offset:16
	v_addc_co_u32_e32 v51, vcc, 0, v51, vcc
	global_load_dwordx4 v[30:33], v[30:31], off offset:48
	s_nop 0
	global_load_dwordx4 v[34:37], v[34:35], off
	s_nop 0
	ds_read_b128 v[38:41], v188 offset:5120
	ds_read_b128 v[42:45], v188 offset:7168
	s_nop 0
	ds_read_b128 v[46:49], v188 offset:6144
	s_lshl_b64 s[0:1], s[0:1], 1
	ds_read_b128 v[50:53], v188 offset:4096
	s_add_u32 s0, s76, s0
	s_addc_u32 s1, s77, s1
	v_lshl_add_u64 v[20:21], v[20:21], 1, s[0:1]
	s_waitcnt lgkmcnt(0)
	s_waitcnt vmcnt(3)
	v_pk_add_f32 v[22:23], v[22:23], 1.0 op_sel_hi:[1,0]
	s_waitcnt lgkmcnt(0)
	s_waitcnt vmcnt(2)
	v_pk_add_f32 v[26:27], v[26:27], 1.0 op_sel_hi:[1,0]
	v_pk_add_f32 v[28:29], v[28:29], 1.0 op_sel_hi:[1,0]
	s_waitcnt lgkmcnt(0)
	s_waitcnt vmcnt(0)
	v_pk_add_f32 v[34:35], v[34:35], 1.0 op_sel_hi:[1,0]
	v_pk_add_f32 v[36:37], v[36:37], 1.0 op_sel_hi:[1,0]
	v_pk_add_f32 v[24:25], v[24:25], 1.0 op_sel_hi:[1,0]
	v_pk_add_f32 v[30:31], v[30:31], 1.0 op_sel_hi:[1,0]
	v_pk_add_f32 v[32:33], v[32:33], 1.0 op_sel_hi:[1,0]
	s_waitcnt lgkmcnt(0)
	s_waitcnt vmcnt(0)
	v_pk_fma_f32 v[8:9], v[8:9], v[26:27], v[38:39]
	v_pk_fma_f32 v[10:11], v[10:11], v[28:29], v[40:41]
	s_waitcnt lgkmcnt(0)
	s_waitcnt vmcnt(0)
	v_pk_fma_f32 v[12:13], v[12:13], v[22:23], v[46:47]
	s_waitcnt lgkmcnt(0)
	s_waitcnt vmcnt(0)
	v_pk_fma_f32 v[4:5], v[4:5], v[34:35], v[50:51]
	v_pk_fma_f32 v[22:23], v[6:7], v[36:37], v[52:53]
	v_pk_fma_f32 v[14:15], v[14:15], v[24:25], v[48:49]
	v_pk_fma_f32 v[16:17], v[16:17], v[30:31], v[42:43]
	v_pk_fma_f32 v[18:19], v[18:19], v[32:33], v[44:45]
	v_cvt_pk_bf16_f32 v6, v8, v9
	v_cvt_pk_bf16_f32 v7, v10, v11
	v_cvt_pk_bf16_f32 v4, v4, v5
	v_cvt_pk_bf16_f32 v5, v22, v23
	v_cvt_pk_bf16_f32 v8, v12, v13
	v_cvt_pk_bf16_f32 v9, v14, v15
	v_cvt_pk_bf16_f32 v10, v16, v17
	v_cvt_pk_bf16_f32 v11, v18, v19
	global_store_dwordx4 v[20:21], v[4:7], off
	global_store_dwordx4 v[20:21], v[8:11], off offset:16
.LBB0_977:
	s_or_b32 s22, s96, 1
	s_add_i32 s0, s22, s35
	s_ashr_i32 s1, s0, 31
	s_lshr_b32 s1, s1, 19
	s_add_i32 s0, s0, s1
	s_ashr_i32 s2, s0, 13
	s_ashr_i32 s0, s2, 31
	s_add_u32 s1, s2, s87
	s_addc_u32 s0, s0, 0
	s_mulk_i32 s0, 0x6000
	s_mul_hi_u32 s3, s1, 0x6000
	v_mov_b32_e32 v4, v179
	s_add_i32 s3, s3, s0
	s_mulk_i32 s1, 0x6000
	s_add_u32 s0, s70, s1
	v_lshlrev_b32_e32 v20, 4, v4
	s_addc_u32 s1, s71, s3
	s_ashr_i32 s23, s22, 31
	v_readlane_b32 s36, v253, 60
	v_ashrrev_i32_e32 v21, 31, v20
	s_lshl_b64 s[26:27], s[22:23], 12
	v_readlane_b32 s38, v253, 62
	v_lshlrev_b64 v[4:5], 2, v[20:21]
	v_readlane_b32 s39, v253, 63
	s_add_u32 s6, s38, s26
	v_lshl_add_u64 v[22:23], s[0:1], 0, v[4:5]
	s_mov_b64 s[0:1], 0x5000
	s_addc_u32 s7, s39, s27
	v_lshl_add_u64 v[14:15], v[22:23], 0, s[0:1]
	s_lshl_b64 s[0:1], s[22:23], 3
	v_add_co_u32_e32 v22, vcc, s18, v22
	s_add_u32 s0, s64, s0
	s_nop 0
	v_addc_co_u32_e32 v23, vcc, 0, v23, vcc
	v_lshl_add_u64 v[18:19], s[6:7], 0, v[4:5]
	s_addc_u32 s1, s65, s1
	ds_read_b128 v[6:9], v188 offset:3072
	ds_read_b128 v[10:13], v188 offset:2048
	s_nop 0
	ds_read_b128 v[14:17], v188 offset:1024
	s_nop 0
	ds_read_b128 v[22:25], v188 offset:0
	s_nop 0
	global_load_dwordx2 v[128:129], v3, s[0:1]
	global_load_dwordx4 v[26:29], v[18:19], off
	global_load_dwordx4 v[30:33], v[18:19], off offset:16
	global_load_dwordx4 v[34:37], v[18:19], off offset:32
	global_load_dwordx4 v[38:41], v[18:19], off offset:48
	v_lshl_add_u64 v[70:71], s[28:29], 0, v[4:5]
	v_lshl_add_u64 v[18:19], s[16:17], 0, v[4:5]
	ds_read_b128 v[42:45], v185 offset:7168
	ds_read_b128 v[46:49], v185 offset:3072
	ds_read_b128 v[50:53], v185 offset:2048
	ds_read_b128 v[54:57], v185 offset:6144
	ds_read_b128 v[58:61], v185 offset:5120
	ds_read_b128 v[62:65], v185 offset:1024
	ds_read_b128 v[66:69], v185 offset:0
	s_nop 0
	ds_read_b128 v[70:73], v185 offset:4096
	v_readlane_b32 s37, v253, 61
	v_readlane_b32 s36, v255, 42
	v_readlane_b32 s24, v255, 23
	v_readlane_b32 s38, v255, 44
	v_readlane_b32 s25, v255, 24
	s_add_u32 s20, s30, s26
	s_addc_u32 s21, s31, s27
	s_andn2_b64 vcc, exec, s[24:25]
	v_readlane_b32 s40, v254, 0
	v_readlane_b32 s41, v254, 1
	v_readlane_b32 s42, v254, 2
	v_readlane_b32 s43, v254, 3
	v_readlane_b32 s44, v254, 4
	v_readlane_b32 s45, v254, 5
	v_readlane_b32 s46, v254, 6
	v_readlane_b32 s47, v254, 7
	v_readlane_b32 s48, v254, 8
	v_readlane_b32 s49, v254, 9
	v_readlane_b32 s50, v254, 10
	v_readlane_b32 s51, v254, 11
	v_readlane_b32 s37, v255, 43
	v_readlane_b32 s39, v255, 45
	s_waitcnt lgkmcnt(0)
	s_waitcnt vmcnt(5)
	v_pk_add_f32 v[18:19], v[24:25], 1.0 op_sel_hi:[1,0]
	v_pk_add_f32 v[22:23], v[22:23], 1.0 op_sel_hi:[1,0]
	s_waitcnt lgkmcnt(0)
	s_waitcnt vmcnt(3)
	v_pk_add_f32 v[24:25], v[26:27], v[128:129] op_sel_hi:[1,0] neg_lo:[0,1] neg_hi:[0,1]
	v_pk_add_f32 v[26:27], v[28:29], v[128:129] op_sel_hi:[1,0] neg_lo:[0,1] neg_hi:[0,1]
	s_waitcnt lgkmcnt(0)
	s_waitcnt vmcnt(2)
	v_pk_add_f32 v[28:29], v[30:31], v[128:129] op_sel_hi:[1,0] neg_lo:[0,1] neg_hi:[0,1]
	v_pk_add_f32 v[30:31], v[32:33], v[128:129] op_sel_hi:[1,0] neg_lo:[0,1] neg_hi:[0,1]
	s_waitcnt lgkmcnt(0)
	s_waitcnt vmcnt(1)
	v_pk_add_f32 v[32:33], v[34:35], v[128:129] op_sel_hi:[1,0] neg_lo:[0,1] neg_hi:[0,1]
	v_pk_add_f32 v[34:35], v[36:37], v[128:129] op_sel_hi:[1,0] neg_lo:[0,1] neg_hi:[0,1]
	s_waitcnt lgkmcnt(0)
	s_waitcnt vmcnt(0)
	v_pk_add_f32 v[36:37], v[38:39], v[128:129] op_sel_hi:[1,0] neg_lo:[0,1] neg_hi:[0,1]
	v_pk_add_f32 v[38:39], v[40:41], v[128:129] op_sel_hi:[1,0] neg_lo:[0,1] neg_hi:[0,1]
	v_pk_mul_f32 v[24:25], v[128:129], v[24:25] op_sel:[1,0]
	v_pk_mul_f32 v[38:39], v[128:129], v[38:39] op_sel:[1,0]
	s_waitcnt lgkmcnt(0)
	s_waitcnt vmcnt(0)
	v_pk_fma_f32 v[24:25], v[66:67], v[24:25], v[70:71]
	v_pk_mul_f32 v[32:33], v[128:129], v[32:33] op_sel:[1,0]
	v_pk_mul_f32 v[26:27], v[128:129], v[26:27] op_sel:[1,0]
	v_pk_fma_f32 v[38:39], v[38:39], v[48:49], v[44:45]
	v_pk_mul_f32 v[24:25], v[24:25], s[34:35] op_sel_hi:[1,0]
	v_pk_add_f32 v[8:9], v[8:9], 1.0 op_sel_hi:[1,0]
	v_pk_mul_f32 v[36:37], v[128:129], v[36:37] op_sel:[1,0]
	v_pk_fma_f32 v[32:33], v[32:33], v[50:51], v[54:55]
	v_pk_fma_f32 v[26:27], v[26:27], v[68:69], v[72:73]
	v_pk_mul_f32 v[38:39], v[38:39], s[34:35] op_sel_hi:[1,0]
	v_pk_fma_f32 v[54:55], v[110:111], v[22:23], v[24:25]
	v_pk_mul_f32 v[34:35], v[128:129], v[34:35] op_sel:[1,0]
	v_pk_mul_f32 v[28:29], v[128:129], v[28:29] op_sel:[1,0]
	v_pk_fma_f32 v[36:37], v[36:37], v[46:47], v[42:43]
	v_pk_mul_f32 v[26:27], v[26:27], s[34:35] op_sel_hi:[1,0]
	v_pk_fma_f32 v[42:43], v[124:125], v[8:9], v[38:39]
	v_add_f32_e32 v8, 0, v54
	v_pk_fma_f32 v[34:35], v[34:35], v[52:53], v[56:57]
	v_pk_fma_f32 v[28:29], v[28:29], v[62:63], v[58:59]
	v_pk_fma_f32 v[52:53], v[112:113], v[18:19], v[26:27]
	v_add_f32_e32 v8, v8, v55
	v_pk_add_f32 v[14:15], v[14:15], 1.0 op_sel_hi:[1,0]
	v_pk_mul_f32 v[30:31], v[128:129], v[30:31] op_sel:[1,0]
	v_pk_mul_f32 v[28:29], v[28:29], s[34:35] op_sel_hi:[1,0]
	v_add_f32_e32 v8, v8, v52
	v_pk_fma_f32 v[30:31], v[30:31], v[64:65], v[60:61]
	v_pk_fma_f32 v[50:51], v[114:115], v[14:15], v[28:29]
	v_add_f32_e32 v8, v8, v53
	v_pk_add_f32 v[16:17], v[16:17], 1.0 op_sel_hi:[1,0]
	v_pk_mul_f32 v[30:31], v[30:31], s[34:35] op_sel_hi:[1,0]
	v_add_f32_e32 v8, v8, v50
	v_pk_fma_f32 v[48:49], v[116:117], v[16:17], v[30:31]
	v_add_f32_e32 v8, v8, v51
	v_pk_add_f32 v[10:11], v[10:11], 1.0 op_sel_hi:[1,0]
	v_pk_mul_f32 v[32:33], v[32:33], s[34:35] op_sel_hi:[1,0]
	v_add_f32_e32 v8, v8, v48
	v_pk_fma_f32 v[46:47], v[118:119], v[10:11], v[32:33]
	v_add_f32_e32 v8, v8, v49
	v_pk_add_f32 v[12:13], v[12:13], 1.0 op_sel_hi:[1,0]
	v_pk_mul_f32 v[34:35], v[34:35], s[34:35] op_sel_hi:[1,0]
	v_add_f32_e32 v8, v8, v46
	v_pk_fma_f32 v[44:45], v[120:121], v[12:13], v[34:35]
	v_add_f32_e32 v8, v8, v47
	v_pk_add_f32 v[6:7], v[6:7], 1.0 op_sel_hi:[1,0]
	v_pk_mul_f32 v[36:37], v[36:37], s[34:35] op_sel_hi:[1,0]
	v_add_f32_e32 v8, v8, v44
	v_pk_fma_f32 v[6:7], v[122:123], v[6:7], v[36:37]
	v_add_f32_e32 v8, v8, v45
	v_add_f32_e32 v8, v8, v6
	v_add_f32_e32 v8, v8, v7
	v_add_f32_e32 v8, v8, v42
	v_add_f32_e32 v8, v8, v43
	ds_bpermute_b32 v9, v2, v8
	v_lshl_add_u64 v[22:23], s[12:13], 0, v[4:5]
	v_lshl_add_u64 v[38:39], s[90:91], 0, v[4:5]
	s_waitcnt lgkmcnt(0)
	v_add_f32_e32 v8, v8, v9
	ds_bpermute_b32 v9, v1, v8
	s_waitcnt lgkmcnt(0)
	v_add_f32_e32 v8, v8, v9
	ds_bpermute_b32 v9, v74, v8
	s_waitcnt lgkmcnt(0)
	v_add_f32_e32 v8, v8, v9
	ds_bpermute_b32 v9, v75, v8
	s_waitcnt lgkmcnt(0)
	v_add_f32_e32 v26, v8, v9
	ds_bpermute_b32 v27, v126, v26
	ds_read_b128 v[8:11], v185 offset:11264
	ds_read_b128 v[12:15], v185 offset:10240
	ds_read_b128 v[16:19], v185 offset:9216
	s_nop 0
	ds_read_b128 v[22:25], v185 offset:8192
	s_waitcnt lgkmcnt(0)
	v_add_f32_e32 v56, v26, v27
	ds_read_b128 v[26:29], v185 offset:15360
	ds_read_b128 v[30:33], v185 offset:14336
	ds_read_b128 v[34:37], v185 offset:13312
	s_nop 0
	ds_read_b128 v[38:41], v185 offset:12288
	ds_bpermute_b32 v57, v127, v56
	s_waitcnt lgkmcnt(0)
	v_add_f32_e32 v56, v56, v57
	v_mul_f32_e32 v56, 0x3a800000, v56
	v_pk_add_f32 v[54:55], v[54:55], v[56:57] op_sel_hi:[1,0] neg_lo:[0,1] neg_hi:[0,1]
	v_pk_add_f32 v[52:53], v[52:53], v[56:57] op_sel_hi:[1,0] neg_lo:[0,1] neg_hi:[0,1]
	v_pk_add_f32 v[50:51], v[50:51], v[56:57] op_sel_hi:[1,0] neg_lo:[0,1] neg_hi:[0,1]
	v_pk_add_f32 v[48:49], v[48:49], v[56:57] op_sel_hi:[1,0] neg_lo:[0,1] neg_hi:[0,1]
	v_pk_add_f32 v[46:47], v[46:47], v[56:57] op_sel_hi:[1,0] neg_lo:[0,1] neg_hi:[0,1]
	v_pk_add_f32 v[44:45], v[44:45], v[56:57] op_sel_hi:[1,0] neg_lo:[0,1] neg_hi:[0,1]
	v_pk_add_f32 v[6:7], v[6:7], v[56:57] op_sel_hi:[1,0] neg_lo:[0,1] neg_hi:[0,1]
	v_pk_add_f32 v[42:43], v[42:43], v[56:57] op_sel_hi:[1,0] neg_lo:[0,1] neg_hi:[0,1]
	v_pk_mul_f32 v[56:57], v[54:55], v[54:55]
	v_pk_mul_f32 v[58:59], v[52:53], v[52:53]
	v_add_f32_e32 v56, v56, v57
	v_add_f32_e32 v56, v58, v56
	v_pk_mul_f32 v[60:61], v[50:51], v[50:51]
	v_add_f32_e32 v56, v59, v56
	v_add_f32_e32 v56, v60, v56
	v_pk_mul_f32 v[62:63], v[48:49], v[48:49]
	v_add_f32_e32 v56, v61, v56
	v_add_f32_e32 v56, v62, v56
	v_pk_mul_f32 v[64:65], v[46:47], v[46:47]
	v_add_f32_e32 v56, v63, v56
	v_add_f32_e32 v56, v64, v56
	v_pk_mul_f32 v[66:67], v[44:45], v[44:45]
	v_add_f32_e32 v56, v65, v56
	v_add_f32_e32 v56, v66, v56
	v_pk_mul_f32 v[68:69], v[6:7], v[6:7]
	v_add_f32_e32 v56, v67, v56
	v_add_f32_e32 v56, v68, v56
	v_pk_mul_f32 v[70:71], v[42:43], v[42:43]
	v_add_f32_e32 v56, v69, v56
	v_add_f32_e32 v56, v70, v56
	v_add_f32_e32 v56, v71, v56
	ds_bpermute_b32 v57, v2, v56
	v_cndmask_b32_e64 v58, 0, 1, s[24:25]
	v_cmp_ne_u32_e64 s[6:7], 1, v58
	s_waitcnt lgkmcnt(0)
	v_add_f32_e32 v56, v56, v57
	ds_bpermute_b32 v57, v1, v56
	s_waitcnt lgkmcnt(0)
	v_add_f32_e32 v56, v56, v57
	ds_bpermute_b32 v57, v74, v56
	s_waitcnt lgkmcnt(0)
	v_add_f32_e32 v56, v56, v57
	ds_bpermute_b32 v57, v75, v56
	s_waitcnt lgkmcnt(0)
	v_add_f32_e32 v56, v56, v57
	ds_bpermute_b32 v57, v126, v56
	s_waitcnt lgkmcnt(0)
	v_add_f32_e32 v56, v56, v57
	ds_bpermute_b32 v57, v127, v56
	s_waitcnt lgkmcnt(0)
	v_add_f32_e32 v56, v56, v57
	v_fmamk_f32 v56, v56, 0x3a800000, v204
	v_mul_f32_e32 v57, 0x4b800000, v56
	v_cmp_gt_f32_e64 s[0:1], s38, v56
	s_nop 1
	v_cndmask_b32_e64 v56, v56, v57, s[0:1]
	v_rsq_f32_e32 v58, v56
	v_lshl_add_u64 v[56:57], s[20:21], 0, v[4:5]
	v_mul_f32_e32 v4, 0x45800000, v58
	v_cndmask_b32_e64 v4, v58, v4, s[0:1]
	v_pk_mul_f32 v[54:55], v[54:55], v[4:5] op_sel_hi:[1,0]
	v_pk_mul_f32 v[52:53], v[52:53], v[4:5] op_sel_hi:[1,0]
	v_pk_mul_f32 v[50:51], v[50:51], v[4:5] op_sel_hi:[1,0]
	v_pk_mul_f32 v[48:49], v[48:49], v[4:5] op_sel_hi:[1,0]
	v_pk_mul_f32 v[46:47], v[46:47], v[4:5] op_sel_hi:[1,0]
	v_pk_mul_f32 v[44:45], v[44:45], v[4:5] op_sel_hi:[1,0]
	v_pk_mul_f32 v[58:59], v[6:7], v[4:5] op_sel_hi:[1,0]
	v_pk_mul_f32 v[42:43], v[42:43], v[4:5] op_sel_hi:[1,0]
	s_waitcnt lgkmcnt(0)
	s_waitcnt vmcnt(0)
	v_pk_fma_f32 v[4:5], v[22:23], v[54:55], v[38:39]
	v_pk_fma_f32 v[6:7], v[24:25], v[52:53], v[40:41]
	v_pk_fma_f32 v[16:17], v[16:17], v[50:51], v[34:35]
	v_pk_fma_f32 v[18:19], v[18:19], v[48:49], v[36:37]
	v_pk_fma_f32 v[12:13], v[12:13], v[46:47], v[30:31]
	v_pk_fma_f32 v[14:15], v[14:15], v[44:45], v[32:33]
	v_pk_fma_f32 v[8:9], v[8:9], v[58:59], v[26:27]
	v_pk_fma_f32 v[10:11], v[10:11], v[42:43], v[28:29]
	global_store_dwordx4 v[56:57], v[4:7], off
	global_store_dwordx4 v[56:57], v[16:19], off offset:16
	global_store_dwordx4 v[56:57], v[12:15], off offset:32
	global_store_dwordx4 v[56:57], v[8:11], off offset:48
	s_cbranch_vccnz .LBB0_979
	s_lshl_b64 s[0:1], s[22:23], 10
	s_mul_hi_i32 s3, s2, 0x6000
	s_mulk_i32 s2, 0x6000
	s_add_u32 s2, s70, s2
	s_addc_u32 s3, s71, s3
	v_lshl_add_u64 v[50:51], v[20:21], 2, s[2:3]
	s_mov_b64 s[2:3], 0x19000
	v_add_co_u32_e32 v34, vcc, s86, v50
	v_lshl_add_u64 v[30:31], v[50:51], 0, s[2:3]
	s_mov_b64 s[2:3], 0x18000
	v_addc_co_u32_e32 v35, vcc, 0, v51, vcc
	v_lshl_add_u64 v[46:47], v[50:51], 0, s[2:3]
	v_add_co_u32_e32 v50, vcc, s67, v50
	global_load_dwordx4 v[22:25], v[30:31], off offset:32
	global_load_dwordx4 v[26:29], v[30:31], off offset:16
	v_addc_co_u32_e32 v51, vcc, 0, v51, vcc
	global_load_dwordx4 v[30:33], v[30:31], off offset:48
	s_nop 0
	global_load_dwordx4 v[34:37], v[34:35], off
	s_nop 0
	ds_read_b128 v[38:41], v188 offset:5120
	ds_read_b128 v[42:45], v188 offset:7168
	s_nop 0
	ds_read_b128 v[46:49], v188 offset:6144
	s_lshl_b64 s[0:1], s[0:1], 1
	ds_read_b128 v[50:53], v188 offset:4096
	s_add_u32 s0, s76, s0
	s_addc_u32 s1, s77, s1
	v_lshl_add_u64 v[20:21], v[20:21], 1, s[0:1]
	s_waitcnt lgkmcnt(0)
	s_waitcnt vmcnt(3)
	v_pk_add_f32 v[22:23], v[22:23], 1.0 op_sel_hi:[1,0]
	s_waitcnt lgkmcnt(0)
	s_waitcnt vmcnt(2)
	v_pk_add_f32 v[26:27], v[26:27], 1.0 op_sel_hi:[1,0]
	v_pk_add_f32 v[28:29], v[28:29], 1.0 op_sel_hi:[1,0]
	s_waitcnt lgkmcnt(0)
	s_waitcnt vmcnt(0)
	v_pk_add_f32 v[34:35], v[34:35], 1.0 op_sel_hi:[1,0]
	v_pk_add_f32 v[36:37], v[36:37], 1.0 op_sel_hi:[1,0]
	v_pk_add_f32 v[24:25], v[24:25], 1.0 op_sel_hi:[1,0]
	v_pk_add_f32 v[30:31], v[30:31], 1.0 op_sel_hi:[1,0]
	v_pk_add_f32 v[32:33], v[32:33], 1.0 op_sel_hi:[1,0]
	s_waitcnt lgkmcnt(0)
	s_waitcnt vmcnt(0)
	v_pk_fma_f32 v[16:17], v[16:17], v[26:27], v[38:39]
	v_pk_fma_f32 v[18:19], v[18:19], v[28:29], v[40:41]
	s_waitcnt lgkmcnt(0)
	s_waitcnt vmcnt(0)
	v_pk_fma_f32 v[4:5], v[4:5], v[34:35], v[50:51]
	v_pk_fma_f32 v[26:27], v[6:7], v[36:37], v[52:53]
	v_pk_fma_f32 v[12:13], v[12:13], v[22:23], v[46:47]
	v_pk_fma_f32 v[14:15], v[14:15], v[24:25], v[48:49]
	v_pk_fma_f32 v[22:23], v[8:9], v[30:31], v[42:43]
	v_pk_fma_f32 v[24:25], v[10:11], v[32:33], v[44:45]
	v_cvt_pk_bf16_f32 v6, v16, v17
	v_cvt_pk_bf16_f32 v7, v18, v19
	v_cvt_pk_bf16_f32 v4, v4, v5
	v_cvt_pk_bf16_f32 v5, v26, v27
	v_cvt_pk_bf16_f32 v8, v12, v13
	v_cvt_pk_bf16_f32 v9, v14, v15
	v_cvt_pk_bf16_f32 v10, v22, v23
	v_cvt_pk_bf16_f32 v11, v24, v25
	global_store_dwordx4 v[20:21], v[4:7], off
	global_store_dwordx4 v[20:21], v[8:11], off offset:16
.LBB0_979:
	s_or_b32 s0, s96, 2
	s_add_i32 s1, s0, s35
	s_ashr_i32 s2, s1, 31
	s_lshr_b32 s2, s2, 19
	s_add_i32 s1, s1, s2
	s_ashr_i32 s2, s1, 13
	s_ashr_i32 s1, s2, 31
	s_add_u32 s3, s2, s87
	s_addc_u32 s1, s1, 0
	s_mulk_i32 s1, 0x6000
	s_mul_hi_u32 s20, s3, 0x6000
	v_mov_b32_e32 v4, v179
	s_add_i32 s1, s20, s1
	s_mulk_i32 s3, 0x6000
	s_add_u32 s20, s70, s3
	v_lshlrev_b32_e32 v52, 4, v4
	s_addc_u32 s21, s71, s1
	s_ashr_i32 s1, s0, 31
	v_readlane_b32 s36, v253, 60
	v_ashrrev_i32_e32 v53, 31, v52
	s_lshl_b64 s[22:23], s[0:1], 12
	v_readlane_b32 s38, v253, 62
	v_lshlrev_b64 v[54:55], 2, v[52:53]
	v_readlane_b32 s39, v253, 63
	s_add_u32 s24, s38, s22
	v_lshl_add_u64 v[20:21], s[20:21], 0, v[54:55]
	s_mov_b64 s[20:21], 0x5000
	s_addc_u32 s25, s39, s23
	v_lshl_add_u64 v[22:23], v[20:21], 0, s[20:21]
	s_lshl_b64 s[20:21], s[0:1], 3
	s_add_u32 s20, s64, s20
	s_addc_u32 s21, s65, s21
	global_load_dwordx2 v[58:59], v3, s[20:21]
	v_lshl_add_u64 v[16:17], s[24:25], 0, v[54:55]
	global_load_dwordx4 v[4:7], v[16:17], off offset:48
	global_load_dwordx4 v[8:11], v[16:17], off offset:32
	global_load_dwordx4 v[12:15], v[16:17], off offset:16
	s_nop 0
	global_load_dwordx4 v[16:19], v[16:17], off
	v_lshl_add_u64 v[24:25], s[16:17], 0, v[54:55]
	v_lshl_add_u64 v[26:27], s[28:29], 0, v[54:55]
	v_lshl_add_u64 v[32:33], s[90:91], 0, v[54:55]
	v_readlane_b32 s24, v255, 42
	v_readlane_b32 s26, v255, 44
	s_add_u32 s20, s30, s22
	s_addc_u32 s21, s31, s23
	v_readlane_b32 s37, v253, 61
	v_readlane_b32 s40, v254, 0
	v_readlane_b32 s41, v254, 1
	v_readlane_b32 s42, v254, 2
	v_readlane_b32 s43, v254, 3
	v_readlane_b32 s44, v254, 4
	v_readlane_b32 s45, v254, 5
	v_readlane_b32 s46, v254, 6
	v_readlane_b32 s47, v254, 7
	v_readlane_b32 s48, v254, 8
	v_readlane_b32 s49, v254, 9
	v_readlane_b32 s50, v254, 10
	v_readlane_b32 s51, v254, 11
	v_readlane_b32 s25, v255, 43
	v_readlane_b32 s27, v255, 45
	s_waitcnt lgkmcnt(0)
	s_waitcnt vmcnt(3)
	v_pk_add_f32 v[62:63], v[4:5], v[58:59] op_sel_hi:[1,0] neg_lo:[0,1] neg_hi:[0,1]
	v_pk_add_f32 v[4:5], v[6:7], v[58:59] op_sel_hi:[1,0] neg_lo:[0,1] neg_hi:[0,1]
	v_add_co_u32_e32 v6, vcc, s18, v20
	s_waitcnt lgkmcnt(0)
	s_waitcnt vmcnt(1)
	v_pk_add_f32 v[70:71], v[14:15], v[58:59] op_sel_hi:[1,0] neg_lo:[0,1] neg_hi:[0,1]
	v_addc_co_u32_e32 v7, vcc, 0, v21, vcc
	ds_read_b128 v[36:39], v188 offset:0
	ds_read_b128 v[110:113], v188 offset:3072
	ds_read_b128 v[114:117], v188 offset:2048
	ds_read_b128 v[44:47], v188 offset:1024
	ds_read_b128 v[118:121], v185 offset:3072
	ds_read_b128 v[122:125], v185 offset:2048
	ds_read_b128 v[48:51], v185 offset:1024
	ds_read_b128 v[40:43], v185 offset:0
	ds_read_b128 v[128:131], v185 offset:7168
	ds_read_b128 v[132:135], v185 offset:6144
	ds_read_b128 v[136:139], v185 offset:5120
	ds_read_b128 v[140:143], v185 offset:4096
	v_pk_mul_f32 v[70:71], v[58:59], v[70:71] op_sel:[1,0]
	v_pk_add_f32 v[66:67], v[12:13], v[58:59] op_sel_hi:[1,0] neg_lo:[0,1] neg_hi:[0,1]
	s_waitcnt lgkmcnt(0)
	s_waitcnt vmcnt(0)
	v_pk_add_f32 v[64:65], v[18:19], v[58:59] op_sel_hi:[1,0] neg_lo:[0,1] neg_hi:[0,1]
	v_pk_add_f32 v[60:61], v[16:17], v[58:59] op_sel_hi:[1,0] neg_lo:[0,1] neg_hi:[0,1]
	v_pk_mul_f32 v[4:5], v[58:59], v[4:5] op_sel:[1,0]
	v_pk_add_f32 v[68:69], v[10:11], v[58:59] op_sel_hi:[1,0] neg_lo:[0,1] neg_hi:[0,1]
	v_pk_mul_f32 v[62:63], v[58:59], v[62:63] op_sel:[1,0]
	v_pk_add_f32 v[72:73], v[8:9], v[58:59] op_sel_hi:[1,0] neg_lo:[0,1] neg_hi:[0,1]
	v_pk_mul_f32 v[68:69], v[58:59], v[68:69] op_sel:[1,0]
	v_pk_mul_f32 v[72:73], v[58:59], v[72:73] op_sel:[1,0]
	v_lshl_add_u64 v[8:9], s[12:13], 0, v[54:55]
	s_waitcnt lgkmcnt(0)
	s_waitcnt vmcnt(0)
	v_pk_add_f32 v[38:39], v[38:39], 1.0 op_sel_hi:[1,0]
	v_pk_add_f32 v[36:37], v[36:37], 1.0 op_sel_hi:[1,0]
	s_waitcnt lgkmcnt(0)
	s_waitcnt vmcnt(0)
	v_pk_add_f32 v[6:7], v[112:113], 1.0 op_sel_hi:[1,0]
	s_waitcnt lgkmcnt(0)
	s_waitcnt vmcnt(0)
	v_pk_add_f32 v[46:47], v[46:47], 1.0 op_sel_hi:[1,0]
	v_pk_add_f32 v[44:45], v[44:45], 1.0 op_sel_hi:[1,0]
	s_waitcnt lgkmcnt(0)
	s_waitcnt vmcnt(0)
	v_pk_fma_f32 v[4:5], v[4:5], v[120:121], v[130:131]
	s_nop 0
	v_pk_mul_f32 v[4:5], v[4:5], s[34:35] op_sel_hi:[1,0]
	s_waitcnt lgkmcnt(0)
	s_waitcnt vmcnt(0)
	v_pk_fma_f32 v[50:51], v[70:71], v[50:51], v[138:139]
	v_pk_fma_f32 v[62:63], v[62:63], v[118:119], v[128:129]
	v_pk_mul_f32 v[50:51], v[50:51], s[34:35] op_sel_hi:[1,0]
	v_pk_fma_f32 v[56:57], v[108:109], v[6:7], v[4:5]
	v_pk_fma_f32 v[46:47], v[100:101], v[46:47], v[50:51]
	v_pk_mul_f32 v[50:51], v[58:59], v[66:67] op_sel:[1,0]
	v_pk_mul_f32 v[62:63], v[62:63], s[34:35] op_sel_hi:[1,0]
	v_pk_fma_f32 v[48:49], v[50:51], v[48:49], v[136:137]
	v_pk_add_f32 v[108:109], v[110:111], 1.0 op_sel_hi:[1,0]
	v_pk_mul_f32 v[48:49], v[48:49], s[34:35] op_sel_hi:[1,0]
	v_pk_fma_f32 v[68:69], v[68:69], v[124:125], v[134:135]
	v_pk_fma_f32 v[44:45], v[98:99], v[44:45], v[48:49]
	v_pk_mul_f32 v[48:49], v[58:59], v[64:65] op_sel:[1,0]
	v_pk_fma_f32 v[62:63], v[106:107], v[108:109], v[62:63]
	s_waitcnt lgkmcnt(0)
	s_waitcnt vmcnt(0)
	v_pk_fma_f32 v[42:43], v[48:49], v[42:43], v[142:143]
	v_pk_mul_f32 v[68:69], v[68:69], s[34:35] op_sel_hi:[1,0]
	v_pk_mul_f32 v[42:43], v[42:43], s[34:35] op_sel_hi:[1,0]
	v_pk_add_f32 v[106:107], v[116:117], 1.0 op_sel_hi:[1,0]
	v_pk_fma_f32 v[38:39], v[96:97], v[38:39], v[42:43]
	v_pk_mul_f32 v[42:43], v[58:59], v[60:61] op_sel:[1,0]
	v_pk_fma_f32 v[72:73], v[72:73], v[122:123], v[132:133]
	v_pk_fma_f32 v[40:41], v[40:41], v[42:43], v[140:141]
	v_pk_fma_f32 v[68:69], v[104:105], v[106:107], v[68:69]
	v_pk_mul_f32 v[40:41], v[40:41], s[34:35] op_sel_hi:[1,0]
	v_pk_mul_f32 v[72:73], v[72:73], s[34:35] op_sel_hi:[1,0]
	v_pk_fma_f32 v[36:37], v[94:95], v[36:37], v[40:41]
	v_pk_add_f32 v[104:105], v[114:115], 1.0 op_sel_hi:[1,0]
	v_add_f32_e32 v40, 0, v36
	v_add_f32_e32 v40, v40, v37
	v_add_f32_e32 v40, v40, v38
	v_add_f32_e32 v40, v40, v39
	v_add_f32_e32 v40, v40, v44
	v_add_f32_e32 v40, v40, v45
	v_add_f32_e32 v40, v40, v46
	v_pk_fma_f32 v[72:73], v[102:103], v[104:105], v[72:73]
	v_add_f32_e32 v40, v40, v47
	v_add_f32_e32 v40, v40, v72
	v_add_f32_e32 v40, v40, v73
	v_add_f32_e32 v40, v40, v68
	v_add_f32_e32 v40, v40, v69
	v_add_f32_e32 v40, v40, v62
	v_add_f32_e32 v40, v40, v63
	v_add_f32_e32 v40, v40, v56
	v_add_f32_e32 v40, v40, v57
	ds_bpermute_b32 v41, v2, v40
	ds_read_b128 v[4:7], v185 offset:11264
	ds_read_b128 v[12:15], v185 offset:10240
	ds_read_b128 v[20:23], v185 offset:9216
	ds_read_b128 v[28:31], v185 offset:8192
	s_nop 0
	ds_read_b128 v[8:11], v185 offset:15360
	ds_read_b128 v[16:19], v185 offset:14336
	ds_read_b128 v[24:27], v185 offset:13312
	s_nop 0
	ds_read_b128 v[32:35], v185 offset:12288
	s_waitcnt lgkmcnt(0)
	v_add_f32_e32 v40, v40, v41
	ds_bpermute_b32 v41, v1, v40
	s_waitcnt lgkmcnt(0)
	v_add_f32_e32 v40, v40, v41
	ds_bpermute_b32 v41, v74, v40
	s_waitcnt lgkmcnt(0)
	v_add_f32_e32 v40, v40, v41
	ds_bpermute_b32 v41, v75, v40
	s_waitcnt lgkmcnt(0)
	v_add_f32_e32 v40, v40, v41
	ds_bpermute_b32 v41, v126, v40
	s_waitcnt lgkmcnt(0)
	v_add_f32_e32 v40, v40, v41
	ds_bpermute_b32 v41, v127, v40
	s_waitcnt lgkmcnt(0)
	v_add_f32_e32 v40, v40, v41
	v_mul_f32_e32 v40, 0x3a800000, v40
	v_pk_add_f32 v[36:37], v[36:37], v[40:41] op_sel_hi:[1,0] neg_lo:[0,1] neg_hi:[0,1]
	v_pk_add_f32 v[38:39], v[38:39], v[40:41] op_sel_hi:[1,0] neg_lo:[0,1] neg_hi:[0,1]
	v_pk_mul_f32 v[42:43], v[36:37], v[36:37]
	v_pk_mul_f32 v[48:49], v[38:39], v[38:39]
	v_add_f32_e32 v42, v42, v43
	v_pk_add_f32 v[44:45], v[44:45], v[40:41] op_sel_hi:[1,0] neg_lo:[0,1] neg_hi:[0,1]
	v_add_f32_e32 v42, v48, v42
	v_pk_mul_f32 v[50:51], v[44:45], v[44:45]
	v_add_f32_e32 v42, v49, v42
	v_pk_add_f32 v[46:47], v[46:47], v[40:41] op_sel_hi:[1,0] neg_lo:[0,1] neg_hi:[0,1]
	v_add_f32_e32 v42, v50, v42
	v_pk_mul_f32 v[58:59], v[46:47], v[46:47]
	v_add_f32_e32 v42, v51, v42
	v_pk_add_f32 v[60:61], v[72:73], v[40:41] op_sel_hi:[1,0] neg_lo:[0,1] neg_hi:[0,1]
	v_add_f32_e32 v42, v58, v42
	v_pk_mul_f32 v[64:65], v[60:61], v[60:61]
	v_add_f32_e32 v42, v59, v42
	v_pk_add_f32 v[66:67], v[68:69], v[40:41] op_sel_hi:[1,0] neg_lo:[0,1] neg_hi:[0,1]
	v_add_f32_e32 v42, v64, v42
	v_pk_mul_f32 v[68:69], v[66:67], v[66:67]
	v_add_f32_e32 v42, v65, v42
	v_pk_add_f32 v[62:63], v[62:63], v[40:41] op_sel_hi:[1,0] neg_lo:[0,1] neg_hi:[0,1]
	v_add_f32_e32 v42, v68, v42
	v_pk_mul_f32 v[70:71], v[62:63], v[62:63]
	v_add_f32_e32 v42, v69, v42
	v_pk_add_f32 v[40:41], v[56:57], v[40:41] op_sel_hi:[1,0] neg_lo:[0,1] neg_hi:[0,1]
	v_add_f32_e32 v42, v70, v42
	v_pk_mul_f32 v[56:57], v[40:41], v[40:41]
	v_add_f32_e32 v42, v71, v42
	v_add_f32_e32 v42, v56, v42
	v_add_f32_e32 v42, v57, v42
	ds_bpermute_b32 v43, v2, v42
	s_waitcnt lgkmcnt(0)
	v_add_f32_e32 v42, v42, v43
	ds_bpermute_b32 v43, v1, v42
	s_waitcnt lgkmcnt(0)
	v_add_f32_e32 v42, v42, v43
	ds_bpermute_b32 v43, v74, v42
	s_waitcnt lgkmcnt(0)
	v_add_f32_e32 v42, v42, v43
	ds_bpermute_b32 v43, v75, v42
	s_waitcnt lgkmcnt(0)
	v_add_f32_e32 v42, v42, v43
	ds_bpermute_b32 v43, v126, v42
	s_waitcnt lgkmcnt(0)
	v_add_f32_e32 v42, v42, v43
	ds_bpermute_b32 v43, v127, v42
	s_waitcnt lgkmcnt(0)
	v_add_f32_e32 v42, v42, v43
	v_fmamk_f32 v42, v42, 0x3a800000, v204
	v_cmp_gt_f32_e32 vcc, s26, v42
	v_mul_f32_e32 v43, 0x4b800000, v42
	s_nop 0
	v_cndmask_b32_e32 v42, v42, v43, vcc
	v_rsq_f32_e32 v42, v42
	s_nop 0
	v_mul_f32_e32 v43, 0x45800000, v42
	v_cndmask_b32_e32 v42, v42, v43, vcc
	v_pk_mul_f32 v[36:37], v[36:37], v[42:43] op_sel_hi:[1,0]
	s_and_b64 vcc, exec, s[6:7]
	s_waitcnt lgkmcnt(0)
	s_waitcnt vmcnt(0)
	v_pk_fma_f32 v[28:29], v[28:29], v[36:37], v[32:33]
	v_pk_mul_f32 v[32:33], v[38:39], v[42:43] op_sel_hi:[1,0]
	s_nop 0
	v_pk_fma_f32 v[30:31], v[30:31], v[32:33], v[34:35]
	v_pk_mul_f32 v[32:33], v[44:45], v[42:43] op_sel_hi:[1,0]
	s_nop 0
	v_pk_fma_f32 v[20:21], v[20:21], v[32:33], v[24:25]
	v_pk_mul_f32 v[24:25], v[46:47], v[42:43] op_sel_hi:[1,0]
	s_nop 0
	v_pk_fma_f32 v[22:23], v[22:23], v[24:25], v[26:27]
	v_pk_mul_f32 v[24:25], v[60:61], v[42:43] op_sel_hi:[1,0]
	s_nop 0
	v_pk_fma_f32 v[12:13], v[12:13], v[24:25], v[16:17]
	v_pk_mul_f32 v[16:17], v[66:67], v[42:43] op_sel_hi:[1,0]
	s_nop 0
	v_pk_fma_f32 v[14:15], v[14:15], v[16:17], v[18:19]
	v_pk_mul_f32 v[16:17], v[62:63], v[42:43] op_sel_hi:[1,0]
	s_nop 0
	v_pk_fma_f32 v[4:5], v[4:5], v[16:17], v[8:9]
	v_pk_mul_f32 v[8:9], v[40:41], v[42:43] op_sel_hi:[1,0]
	s_nop 0
	v_pk_fma_f32 v[6:7], v[6:7], v[8:9], v[10:11]
	v_lshl_add_u64 v[8:9], s[20:21], 0, v[54:55]
	global_store_dwordx4 v[8:9], v[28:31], off
	global_store_dwordx4 v[8:9], v[20:23], off offset:16
	global_store_dwordx4 v[8:9], v[12:15], off offset:32
	global_store_dwordx4 v[8:9], v[4:7], off offset:48
	s_cbranch_vccnz .LBB0_981
	s_lshl_b64 s[0:1], s[0:1], 10
	s_mul_hi_i32 s3, s2, 0x6000
	s_mulk_i32 s2, 0x6000
	s_add_u32 s2, s70, s2
	s_addc_u32 s3, s71, s3
	v_lshl_add_u64 v[48:49], v[52:53], 2, s[2:3]
	s_mov_b64 s[2:3], 0x19000
	v_add_co_u32_e32 v32, vcc, s86, v48
	v_lshl_add_u64 v[24:25], v[48:49], 0, s[2:3]
	s_mov_b64 s[2:3], 0x18000
	v_addc_co_u32_e32 v33, vcc, 0, v49, vcc
	v_lshl_add_u64 v[44:45], v[48:49], 0, s[2:3]
	v_add_co_u32_e32 v48, vcc, s67, v48
	global_load_dwordx4 v[8:11], v[24:25], off offset:32
	global_load_dwordx4 v[16:19], v[24:25], off offset:16
	v_addc_co_u32_e32 v49, vcc, 0, v49, vcc
	global_load_dwordx4 v[24:27], v[24:25], off offset:48
	s_nop 0
	global_load_dwordx4 v[32:35], v[32:33], off
	s_nop 0
	ds_read_b128 v[36:39], v188 offset:5120
	ds_read_b128 v[40:43], v188 offset:7168
	s_nop 0
	ds_read_b128 v[44:47], v188 offset:6144
	s_lshl_b64 s[0:1], s[0:1], 1
	ds_read_b128 v[48:51], v188 offset:4096
	s_add_u32 s0, s76, s0
	s_addc_u32 s1, s77, s1
	v_lshl_add_u64 v[52:53], v[52:53], 1, s[0:1]
	s_waitcnt lgkmcnt(0)
	s_waitcnt vmcnt(3)
	v_pk_add_f32 v[8:9], v[8:9], 1.0 op_sel_hi:[1,0]
	s_waitcnt lgkmcnt(0)
	s_waitcnt vmcnt(2)
	v_pk_add_f32 v[16:17], v[16:17], 1.0 op_sel_hi:[1,0]
	v_pk_add_f32 v[18:19], v[18:19], 1.0 op_sel_hi:[1,0]
	v_pk_add_f32 v[10:11], v[10:11], 1.0 op_sel_hi:[1,0]
	s_waitcnt lgkmcnt(0)
	s_waitcnt vmcnt(1)
	v_pk_add_f32 v[24:25], v[24:25], 1.0 op_sel_hi:[1,0]
	s_waitcnt lgkmcnt(0)
	s_waitcnt vmcnt(0)
	v_pk_add_f32 v[32:33], v[32:33], 1.0 op_sel_hi:[1,0]
	v_pk_add_f32 v[34:35], v[34:35], 1.0 op_sel_hi:[1,0]
	v_pk_add_f32 v[26:27], v[26:27], 1.0 op_sel_hi:[1,0]
	s_waitcnt lgkmcnt(0)
	s_waitcnt vmcnt(0)
	v_pk_fma_f32 v[16:17], v[20:21], v[16:17], v[36:37]
	v_pk_fma_f32 v[18:19], v[22:23], v[18:19], v[38:39]
	s_waitcnt lgkmcnt(0)
	s_waitcnt vmcnt(0)
	v_pk_fma_f32 v[8:9], v[12:13], v[8:9], v[44:45]
	v_pk_fma_f32 v[10:11], v[14:15], v[10:11], v[46:47]
	v_pk_fma_f32 v[4:5], v[4:5], v[24:25], v[40:41]
	s_waitcnt lgkmcnt(0)
	s_waitcnt vmcnt(0)
	v_pk_fma_f32 v[14:15], v[28:29], v[32:33], v[48:49]
	v_pk_fma_f32 v[20:21], v[30:31], v[34:35], v[50:51]
	v_pk_fma_f32 v[12:13], v[6:7], v[26:27], v[42:43]
	v_cvt_pk_bf16_f32 v6, v16, v17
	v_cvt_pk_bf16_f32 v7, v18, v19
	v_cvt_pk_bf16_f32 v8, v8, v9
	v_cvt_pk_bf16_f32 v9, v10, v11
	v_cvt_pk_bf16_f32 v10, v4, v5
	v_cvt_pk_bf16_f32 v4, v14, v15
	v_cvt_pk_bf16_f32 v5, v20, v21
	v_cvt_pk_bf16_f32 v11, v12, v13
	global_store_dwordx4 v[52:53], v[4:7], off
	global_store_dwordx4 v[52:53], v[8:11], off offset:16
.LBB0_981:
	s_or_b32 s22, s96, 3
	s_add_i32 s0, s22, s35
	s_ashr_i32 s1, s0, 31
	s_lshr_b32 s1, s1, 19
	s_add_i32 s0, s0, s1
	s_ashr_i32 s2, s0, 13
	s_ashr_i32 s0, s2, 31
	s_add_u32 s1, s2, s87
	s_addc_u32 s0, s0, 0
	s_mulk_i32 s0, 0x6000
	s_mul_hi_u32 s3, s1, 0x6000
	v_mov_b32_e32 v4, v179
	s_add_i32 s3, s3, s0
	s_mulk_i32 s1, 0x6000
	s_add_u32 s0, s70, s1
	v_lshlrev_b32_e32 v20, 4, v4
	s_addc_u32 s1, s71, s3
	s_ashr_i32 s23, s22, 31
	v_readlane_b32 s36, v253, 60
	v_ashrrev_i32_e32 v21, 31, v20
	s_lshl_b64 s[26:27], s[22:23], 12
	v_readlane_b32 s38, v253, 62
	v_lshlrev_b64 v[4:5], 2, v[20:21]
	v_readlane_b32 s39, v253, 63
	s_add_u32 s20, s38, s26
	v_lshl_add_u64 v[22:23], s[0:1], 0, v[4:5]
	s_mov_b64 s[0:1], 0x5000
	s_addc_u32 s21, s39, s27
	v_lshl_add_u64 v[14:15], v[22:23], 0, s[0:1]
	s_lshl_b64 s[0:1], s[22:23], 3
	v_add_co_u32_e32 v22, vcc, s18, v22
	s_add_u32 s0, s64, s0
	s_nop 0
	v_addc_co_u32_e32 v23, vcc, 0, v23, vcc
	v_lshl_add_u64 v[18:19], s[20:21], 0, v[4:5]
	s_addc_u32 s1, s65, s1
	ds_read_b128 v[6:9], v188 offset:3072
	ds_read_b128 v[10:13], v188 offset:2048
	s_nop 0
	ds_read_b128 v[14:17], v188 offset:1024
	s_nop 0
	ds_read_b128 v[22:25], v188 offset:0
	s_nop 0
	global_load_dwordx2 v[94:95], v3, s[0:1]
	global_load_dwordx4 v[26:29], v[18:19], off
	global_load_dwordx4 v[30:33], v[18:19], off offset:16
	global_load_dwordx4 v[34:37], v[18:19], off offset:32
	global_load_dwordx4 v[38:41], v[18:19], off offset:48
	v_lshl_add_u64 v[70:71], s[28:29], 0, v[4:5]
	v_lshl_add_u64 v[18:19], s[16:17], 0, v[4:5]
	ds_read_b128 v[42:45], v185 offset:7168
	ds_read_b128 v[46:49], v185 offset:3072
	ds_read_b128 v[50:53], v185 offset:2048
	ds_read_b128 v[54:57], v185 offset:6144
	ds_read_b128 v[58:61], v185 offset:5120
	ds_read_b128 v[62:65], v185 offset:1024
	ds_read_b128 v[66:69], v185 offset:0
	s_nop 0
	ds_read_b128 v[70:73], v185 offset:4096
	v_readlane_b32 s40, v254, 0
	v_readlane_b32 s41, v254, 1
	v_readlane_b32 s42, v254, 2
	v_readlane_b32 s43, v254, 3
	v_readlane_b32 s40, v255, 42
	v_readlane_b32 s42, v255, 44
	s_add_u32 s20, s30, s26
	s_addc_u32 s21, s31, s27
	v_readlane_b32 s43, v255, 45
	s_and_b64 vcc, exec, s[6:7]
	v_readlane_b32 s37, v253, 61
	v_readlane_b32 s44, v254, 4
	v_readlane_b32 s45, v254, 5
	v_readlane_b32 s46, v254, 6
	v_readlane_b32 s47, v254, 7
	v_readlane_b32 s48, v254, 8
	v_readlane_b32 s49, v254, 9
	v_readlane_b32 s50, v254, 10
	v_readlane_b32 s51, v254, 11
	v_readlane_b32 s41, v255, 43
	s_waitcnt lgkmcnt(0)
	s_waitcnt vmcnt(5)
	v_pk_add_f32 v[18:19], v[24:25], 1.0 op_sel_hi:[1,0]
	v_pk_add_f32 v[22:23], v[22:23], 1.0 op_sel_hi:[1,0]
	s_waitcnt lgkmcnt(0)
	s_waitcnt vmcnt(3)
	v_pk_add_f32 v[24:25], v[26:27], v[94:95] op_sel_hi:[1,0] neg_lo:[0,1] neg_hi:[0,1]
	v_pk_add_f32 v[26:27], v[28:29], v[94:95] op_sel_hi:[1,0] neg_lo:[0,1] neg_hi:[0,1]
	s_waitcnt lgkmcnt(0)
	s_waitcnt vmcnt(2)
	v_pk_add_f32 v[28:29], v[30:31], v[94:95] op_sel_hi:[1,0] neg_lo:[0,1] neg_hi:[0,1]
	v_pk_add_f32 v[30:31], v[32:33], v[94:95] op_sel_hi:[1,0] neg_lo:[0,1] neg_hi:[0,1]
	s_waitcnt lgkmcnt(0)
	s_waitcnt vmcnt(1)
	v_pk_add_f32 v[32:33], v[34:35], v[94:95] op_sel_hi:[1,0] neg_lo:[0,1] neg_hi:[0,1]
	v_pk_add_f32 v[34:35], v[36:37], v[94:95] op_sel_hi:[1,0] neg_lo:[0,1] neg_hi:[0,1]
	s_waitcnt lgkmcnt(0)
	s_waitcnt vmcnt(0)
	v_pk_add_f32 v[36:37], v[38:39], v[94:95] op_sel_hi:[1,0] neg_lo:[0,1] neg_hi:[0,1]
	v_pk_add_f32 v[38:39], v[40:41], v[94:95] op_sel_hi:[1,0] neg_lo:[0,1] neg_hi:[0,1]
	v_pk_mul_f32 v[24:25], v[94:95], v[24:25] op_sel:[1,0]
	v_pk_mul_f32 v[38:39], v[94:95], v[38:39] op_sel:[1,0]
	s_waitcnt lgkmcnt(0)
	s_waitcnt vmcnt(0)
	v_pk_fma_f32 v[24:25], v[66:67], v[24:25], v[70:71]
	v_pk_mul_f32 v[32:33], v[94:95], v[32:33] op_sel:[1,0]
	v_pk_mul_f32 v[26:27], v[94:95], v[26:27] op_sel:[1,0]
	v_pk_fma_f32 v[38:39], v[38:39], v[48:49], v[44:45]
	v_pk_mul_f32 v[24:25], v[24:25], s[34:35] op_sel_hi:[1,0]
	v_pk_add_f32 v[8:9], v[8:9], 1.0 op_sel_hi:[1,0]
	v_pk_mul_f32 v[36:37], v[94:95], v[36:37] op_sel:[1,0]
	v_pk_fma_f32 v[32:33], v[32:33], v[50:51], v[54:55]
	v_pk_fma_f32 v[26:27], v[26:27], v[68:69], v[72:73]
	v_pk_mul_f32 v[38:39], v[38:39], s[34:35] op_sel_hi:[1,0]
	v_pk_fma_f32 v[54:55], v[78:79], v[22:23], v[24:25]
	v_pk_mul_f32 v[34:35], v[94:95], v[34:35] op_sel:[1,0]
	v_pk_mul_f32 v[28:29], v[94:95], v[28:29] op_sel:[1,0]
	v_pk_fma_f32 v[36:37], v[36:37], v[46:47], v[42:43]
	v_pk_mul_f32 v[26:27], v[26:27], s[34:35] op_sel_hi:[1,0]
	v_pk_fma_f32 v[42:43], v[84:85], v[8:9], v[38:39]
	v_add_f32_e32 v8, 0, v54
	v_pk_fma_f32 v[34:35], v[34:35], v[52:53], v[56:57]
	v_pk_fma_f32 v[28:29], v[28:29], v[62:63], v[58:59]
	v_pk_fma_f32 v[52:53], v[80:81], v[18:19], v[26:27]
	v_add_f32_e32 v8, v8, v55
	v_pk_add_f32 v[14:15], v[14:15], 1.0 op_sel_hi:[1,0]
	v_pk_mul_f32 v[30:31], v[94:95], v[30:31] op_sel:[1,0]
	v_pk_mul_f32 v[28:29], v[28:29], s[34:35] op_sel_hi:[1,0]
	v_add_f32_e32 v8, v8, v52
	v_pk_fma_f32 v[30:31], v[30:31], v[64:65], v[60:61]
	v_pk_fma_f32 v[50:51], v[82:83], v[14:15], v[28:29]
	v_add_f32_e32 v8, v8, v53
	v_pk_add_f32 v[16:17], v[16:17], 1.0 op_sel_hi:[1,0]
	v_pk_mul_f32 v[30:31], v[30:31], s[34:35] op_sel_hi:[1,0]
	v_add_f32_e32 v8, v8, v50
	v_pk_fma_f32 v[48:49], v[86:87], v[16:17], v[30:31]
	v_add_f32_e32 v8, v8, v51
	v_pk_add_f32 v[10:11], v[10:11], 1.0 op_sel_hi:[1,0]
	v_pk_mul_f32 v[32:33], v[32:33], s[34:35] op_sel_hi:[1,0]
	v_add_f32_e32 v8, v8, v48
	v_pk_fma_f32 v[46:47], v[88:89], v[10:11], v[32:33]
	v_add_f32_e32 v8, v8, v49
	v_pk_add_f32 v[12:13], v[12:13], 1.0 op_sel_hi:[1,0]
	v_pk_mul_f32 v[34:35], v[34:35], s[34:35] op_sel_hi:[1,0]
	v_add_f32_e32 v8, v8, v46
	v_pk_fma_f32 v[44:45], v[90:91], v[12:13], v[34:35]
	v_add_f32_e32 v8, v8, v47
	v_pk_add_f32 v[6:7], v[6:7], 1.0 op_sel_hi:[1,0]
	v_pk_mul_f32 v[36:37], v[36:37], s[34:35] op_sel_hi:[1,0]
	v_add_f32_e32 v8, v8, v44
	v_pk_fma_f32 v[6:7], v[92:93], v[6:7], v[36:37]
	v_add_f32_e32 v8, v8, v45
	v_add_f32_e32 v8, v8, v6
	v_add_f32_e32 v8, v8, v7
	v_add_f32_e32 v8, v8, v42
	v_add_f32_e32 v8, v8, v43
	ds_bpermute_b32 v9, v2, v8
	v_lshl_add_u64 v[22:23], s[12:13], 0, v[4:5]
	v_lshl_add_u64 v[38:39], s[90:91], 0, v[4:5]
	s_waitcnt lgkmcnt(0)
	v_add_f32_e32 v8, v8, v9
	ds_bpermute_b32 v9, v1, v8
	s_waitcnt lgkmcnt(0)
	v_add_f32_e32 v8, v8, v9
	ds_bpermute_b32 v9, v74, v8
	s_waitcnt lgkmcnt(0)
	v_add_f32_e32 v8, v8, v9
	ds_bpermute_b32 v9, v75, v8
	s_waitcnt lgkmcnt(0)
	v_add_f32_e32 v26, v8, v9
	ds_bpermute_b32 v27, v126, v26
	ds_read_b128 v[8:11], v185 offset:11264
	ds_read_b128 v[12:15], v185 offset:10240
	ds_read_b128 v[16:19], v185 offset:9216
	s_nop 0
	ds_read_b128 v[22:25], v185 offset:8192
	s_waitcnt lgkmcnt(0)
	v_add_f32_e32 v56, v26, v27
	ds_read_b128 v[26:29], v185 offset:15360
	ds_read_b128 v[30:33], v185 offset:14336
	ds_read_b128 v[34:37], v185 offset:13312
	s_nop 0
	ds_read_b128 v[38:41], v185 offset:12288
	ds_bpermute_b32 v57, v127, v56
	s_waitcnt lgkmcnt(0)
	v_add_f32_e32 v56, v56, v57
	v_mul_f32_e32 v56, 0x3a800000, v56
	v_pk_add_f32 v[54:55], v[54:55], v[56:57] op_sel_hi:[1,0] neg_lo:[0,1] neg_hi:[0,1]
	v_pk_add_f32 v[52:53], v[52:53], v[56:57] op_sel_hi:[1,0] neg_lo:[0,1] neg_hi:[0,1]
	v_pk_add_f32 v[50:51], v[50:51], v[56:57] op_sel_hi:[1,0] neg_lo:[0,1] neg_hi:[0,1]
	v_pk_add_f32 v[48:49], v[48:49], v[56:57] op_sel_hi:[1,0] neg_lo:[0,1] neg_hi:[0,1]
	v_pk_add_f32 v[46:47], v[46:47], v[56:57] op_sel_hi:[1,0] neg_lo:[0,1] neg_hi:[0,1]
	v_pk_add_f32 v[44:45], v[44:45], v[56:57] op_sel_hi:[1,0] neg_lo:[0,1] neg_hi:[0,1]
	v_pk_add_f32 v[6:7], v[6:7], v[56:57] op_sel_hi:[1,0] neg_lo:[0,1] neg_hi:[0,1]
	v_pk_add_f32 v[42:43], v[42:43], v[56:57] op_sel_hi:[1,0] neg_lo:[0,1] neg_hi:[0,1]
	v_pk_mul_f32 v[56:57], v[54:55], v[54:55]
	v_pk_mul_f32 v[58:59], v[52:53], v[52:53]
	v_add_f32_e32 v56, v56, v57
	v_add_f32_e32 v56, v58, v56
	v_pk_mul_f32 v[60:61], v[50:51], v[50:51]
	v_add_f32_e32 v56, v59, v56
	v_add_f32_e32 v56, v60, v56
	v_pk_mul_f32 v[62:63], v[48:49], v[48:49]
	v_add_f32_e32 v56, v61, v56
	v_add_f32_e32 v56, v62, v56
	v_pk_mul_f32 v[64:65], v[46:47], v[46:47]
	v_add_f32_e32 v56, v63, v56
	v_add_f32_e32 v56, v64, v56
	v_pk_mul_f32 v[66:67], v[44:45], v[44:45]
	v_add_f32_e32 v56, v65, v56
	v_add_f32_e32 v56, v66, v56
	v_pk_mul_f32 v[68:69], v[6:7], v[6:7]
	v_add_f32_e32 v56, v67, v56
	v_add_f32_e32 v56, v68, v56
	v_pk_mul_f32 v[70:71], v[42:43], v[42:43]
	v_add_f32_e32 v56, v69, v56
	v_add_f32_e32 v56, v70, v56
	v_add_f32_e32 v56, v71, v56
	ds_bpermute_b32 v2, v2, v56
	s_waitcnt lgkmcnt(0)
	v_add_f32_e32 v2, v56, v2
	ds_bpermute_b32 v1, v1, v2
	v_lshl_add_u64 v[56:57], s[20:21], 0, v[4:5]
	s_waitcnt lgkmcnt(0)
	v_add_f32_e32 v1, v2, v1
	ds_bpermute_b32 v2, v74, v1
	s_waitcnt lgkmcnt(0)
	v_add_f32_e32 v1, v1, v2
	ds_bpermute_b32 v2, v75, v1
	s_waitcnt lgkmcnt(0)
	v_add_f32_e32 v1, v1, v2
	ds_bpermute_b32 v2, v126, v1
	s_waitcnt lgkmcnt(0)
	v_add_f32_e32 v1, v1, v2
	ds_bpermute_b32 v2, v127, v1
	s_waitcnt lgkmcnt(0)
	v_add_f32_e32 v1, v1, v2
	v_fmamk_f32 v1, v1, 0x3a800000, v204
	v_mul_f32_e32 v2, 0x4b800000, v1
	v_cmp_gt_f32_e64 s[0:1], s42, v1
	s_nop 1
	v_cndmask_b32_e64 v1, v1, v2, s[0:1]
	v_rsq_f32_e32 v1, v1
	s_nop 0
	v_mul_f32_e32 v2, 0x45800000, v1
	v_cndmask_b32_e64 v2, v1, v2, s[0:1]
	v_pk_mul_f32 v[4:5], v[54:55], v[2:3] op_sel_hi:[1,0]
	v_pk_mul_f32 v[52:53], v[52:53], v[2:3] op_sel_hi:[1,0]
	v_pk_mul_f32 v[50:51], v[50:51], v[2:3] op_sel_hi:[1,0]
	v_pk_mul_f32 v[48:49], v[48:49], v[2:3] op_sel_hi:[1,0]
	v_pk_mul_f32 v[46:47], v[46:47], v[2:3] op_sel_hi:[1,0]
	v_pk_mul_f32 v[44:45], v[44:45], v[2:3] op_sel_hi:[1,0]
	v_pk_mul_f32 v[54:55], v[6:7], v[2:3] op_sel_hi:[1,0]
	v_pk_mul_f32 v[42:43], v[42:43], v[2:3] op_sel_hi:[1,0]
	s_waitcnt lgkmcnt(0)
	s_waitcnt vmcnt(0)
	v_pk_fma_f32 v[4:5], v[22:23], v[4:5], v[38:39]
	v_pk_fma_f32 v[6:7], v[24:25], v[52:53], v[40:41]
	v_pk_fma_f32 v[16:17], v[16:17], v[50:51], v[34:35]
	v_pk_fma_f32 v[18:19], v[18:19], v[48:49], v[36:37]
	v_pk_fma_f32 v[12:13], v[12:13], v[46:47], v[30:31]
	v_pk_fma_f32 v[14:15], v[14:15], v[44:45], v[32:33]
	v_pk_fma_f32 v[8:9], v[8:9], v[54:55], v[26:27]
	v_pk_fma_f32 v[10:11], v[10:11], v[42:43], v[28:29]
	global_store_dwordx4 v[56:57], v[4:7], off
	global_store_dwordx4 v[56:57], v[16:19], off offset:16
	global_store_dwordx4 v[56:57], v[12:15], off offset:32
	global_store_dwordx4 v[56:57], v[8:11], off offset:48
	s_cbranch_vccnz .LBB0_937
	s_lshl_b64 s[0:1], s[22:23], 10
	s_mul_hi_i32 s3, s2, 0x6000
	s_mulk_i32 s2, 0x6000
	s_add_u32 s2, s70, s2
	s_addc_u32 s3, s71, s3
	v_lshl_add_u64 v[50:51], v[20:21], 2, s[2:3]
	s_mov_b64 s[2:3], 0x19000
	v_add_co_u32_e32 v34, vcc, s86, v50
	v_lshl_add_u64 v[30:31], v[50:51], 0, s[2:3]
	s_mov_b64 s[2:3], 0x18000
	v_addc_co_u32_e32 v35, vcc, 0, v51, vcc
	v_lshl_add_u64 v[46:47], v[50:51], 0, s[2:3]
	v_add_co_u32_e32 v50, vcc, s67, v50
	global_load_dwordx4 v[22:25], v[30:31], off offset:32
	global_load_dwordx4 v[26:29], v[30:31], off offset:16
	v_addc_co_u32_e32 v51, vcc, 0, v51, vcc
	global_load_dwordx4 v[30:33], v[30:31], off offset:48
	s_nop 0
	global_load_dwordx4 v[34:37], v[34:35], off
	s_nop 0
	ds_read_b128 v[38:41], v188 offset:5120
	ds_read_b128 v[42:45], v188 offset:7168
	s_nop 0
	ds_read_b128 v[46:49], v188 offset:6144
	s_lshl_b64 s[0:1], s[0:1], 1
	ds_read_b128 v[50:53], v188 offset:4096
	s_add_u32 s0, s76, s0
	s_addc_u32 s1, s77, s1
	v_lshl_add_u64 v[20:21], v[20:21], 1, s[0:1]
	s_waitcnt lgkmcnt(0)
	s_waitcnt vmcnt(3)
	v_pk_add_f32 v[22:23], v[22:23], 1.0 op_sel_hi:[1,0]
	s_waitcnt lgkmcnt(0)
	s_waitcnt vmcnt(2)
	v_pk_add_f32 v[26:27], v[26:27], 1.0 op_sel_hi:[1,0]
	v_pk_add_f32 v[28:29], v[28:29], 1.0 op_sel_hi:[1,0]
	s_waitcnt lgkmcnt(0)
	s_waitcnt vmcnt(0)
	v_pk_add_f32 v[34:35], v[34:35], 1.0 op_sel_hi:[1,0]
	v_pk_add_f32 v[36:37], v[36:37], 1.0 op_sel_hi:[1,0]
	v_pk_add_f32 v[24:25], v[24:25], 1.0 op_sel_hi:[1,0]
	v_pk_add_f32 v[30:31], v[30:31], 1.0 op_sel_hi:[1,0]
	v_pk_add_f32 v[32:33], v[32:33], 1.0 op_sel_hi:[1,0]
	s_waitcnt lgkmcnt(0)
	s_waitcnt vmcnt(0)
	v_pk_fma_f32 v[16:17], v[16:17], v[26:27], v[38:39]
	v_pk_fma_f32 v[18:19], v[18:19], v[28:29], v[40:41]
	s_waitcnt lgkmcnt(0)
	s_waitcnt vmcnt(0)
	v_pk_fma_f32 v[4:5], v[4:5], v[34:35], v[50:51]
	v_pk_fma_f32 v[26:27], v[6:7], v[36:37], v[52:53]
	v_pk_fma_f32 v[12:13], v[12:13], v[22:23], v[46:47]
	v_pk_fma_f32 v[14:15], v[14:15], v[24:25], v[48:49]
	v_pk_fma_f32 v[22:23], v[8:9], v[30:31], v[42:43]
	v_pk_fma_f32 v[24:25], v[10:11], v[32:33], v[44:45]
	v_cvt_pk_bf16_f32 v6, v16, v17
	v_cvt_pk_bf16_f32 v7, v18, v19
	v_cvt_pk_bf16_f32 v4, v4, v5
	v_cvt_pk_bf16_f32 v5, v26, v27
	v_cvt_pk_bf16_f32 v8, v12, v13
	v_cvt_pk_bf16_f32 v9, v14, v15
	v_cvt_pk_bf16_f32 v10, v22, v23
	v_cvt_pk_bf16_f32 v11, v24, v25
	global_store_dwordx4 v[20:21], v[4:7], off
	global_store_dwordx4 v[20:21], v[8:11], off offset:16
	s_branch .LBB0_937
